# dense attention: transposed dword epilogue stores for both dense bodies + K-fragment LDS waits moved to first consumer
# speedup vs baseline: 1.0068x; 1.0068x over previous
; template <int NKS, bool MACC>
; __device__ __forceinline__ void qkt8d(f32x16& p0, f32x16& p1, const f32x16& mneg, LAS unsigned char* ldsl, int kb, int rb, const i32x8* qf) {
;     i32x8 a0[2], a1[2];
; #pragma unroll
;     for (int sK = 0; sK < 2; ++sK) {
;         { const i32x4 lo = LDS16(kb ^ (64 * sK)), hh = LDS16(kb ^ (64 * sK + 16)); a0[sK] = __builtin_shufflevector(lo, hh, 0, 1, 2, 3, 4, 5, 6, 7); }
;         { const i32x4 lo = LDS16((kb ^ (64 * sK)) + 4096), hh = LDS16((kb ^ (64 * sK + 16)) + 4096); a1[sK] = __builtin_shufflevector(lo, hh, 0, 1, 2, 3, 4, 5, 6, 7); } }
;     asm volatile("s_waitcnt lgkmcnt(0)" ::: "memory"); SBAR();
;     if constexpr (MACC) {
;         asm volatile("v_mfma_f32_32x32x64_f8f6f4 %0, %1, %2, %3" : "=&v"(p0) : "v"(a0[0]), "v"(qf[0]), "v"(mneg));
;         asm volatile("v_mfma_f32_32x32x64_f8f6f4 %0, %1, %2, %3" : "=&v"(p1) : "v"(a1[0]), "v"(qf[0]), "v"(mneg)); }
;     else { p0 = f32x16{}; p1 = f32x16{}; p0 = D8_MX(a0[0], qf[0], p0); p1 = D8_MX(a1[0], qf[0], p1); }
;     if constexpr (NKS == 3) { i32x8 r0, r1;
;         { const i32x4 lo = LDS16(rb), hh = LDS16(rb ^ 16); r0 = __builtin_shufflevector(lo, hh, 0, 1, 2, 3, 4, 5, 6, 7); }
;         { const i32x4 lo = LDS16(rb + 2048), hh = LDS16((rb ^ 16) + 2048); r1 = __builtin_shufflevector(lo, hh, 0, 1, 2, 3, 4, 5, 6, 7); }
;         p0 = D8_MX(a0[1], qf[1], p0); p1 = D8_MX(a1[1], qf[1], p1);
;         p0 = D8_MX(r0, qf[2], p0); p1 = D8_MX(r1, qf[2], p1); }
;     else { p0 = D8_MX(a0[1], qf[1], p0); p1 = D8_MX(a1[1], qf[1], p1); }
;     if constexpr (MACC) asm volatile("" : "+v"(p1), "+v"(p0) : "v"(mneg));
; }
; __device__ __forceinline__ void pv8d(f32x16* o, LAS unsigned char* ldsl, int vb, const i32x8 pa) {
;     i32x8 bfr[4];
; #pragma unroll
;     for (int d0 = 0; d0 < 4; ++d0) { const i32x4 lo = LDS16(vb + d0 * 2048), hh = LDS16((vb ^ 16) + d0 * 2048); bfr[d0] = __builtin_shufflevector(lo, hh, 0, 1, 2, 3, 4, 5, 6, 7); }
;     asm volatile("s_waitcnt lgkmcnt(0)" ::: "memory"); SBAR();
; #pragma unroll
;     for (int d0 = 0; d0 < 4; ++d0) o[d0] = D8_MX(pa, bfr[d0], o[d0]);
; }
; template <int NKS, bool MACC>
; __device__ __forceinline__ void attn_dense8_dma(int wv, const D8Args a, LAS unsigned char* ldsl) {
;     ...
;         SBAR(); D8Qm(pA0, pA1, 2 * sb);
;         D8Fm(pB0, pB1, alB); SBAR();
;         D8Vm(2 * sbp + 1); D8Pm(false, pA0, pA1, alA);
;         RESC8(alA);
.LBB0_465:
	s_lshl_b32 s23, s15, 14
	v_or_b32_e32 v65, s23, v202
	v_add_u32_e32 v66, 0, v65
	v_xad_u32 v67, v65, 16, 0
	ds_read_b128 v[96:99], v66
	ds_read_b128 v[158:161], v66 offset:4096
	ds_read_b128 v[100:103], v67
	ds_read_b128 v[162:165], v67 offset:4096
	v_xad_u32 v65, v65, 64, 0
	v_bitop3_b32 v66, s23, v242, v202 bitop3:0x36
	v_add_u32_e32 v66, 0, v66
	ds_read_b128 v[104:107], v65
	ds_read_b128 v[166:169], v65 offset:4096
	ds_read_b128 v[108:111], v66
	ds_read_b128 v[170:173], v66 offset:4096
	s_lshl_b32 s0, s15, 13
	v_add_u32_e32 v132, s0, v151
	v_mov_b32_e32 v65, v64
	v_mov_b32_e32 v66, v64
	v_mov_b32_e32 v67, v64
	v_mov_b32_e32 v68, v64
	v_mov_b32_e32 v69, v64
	v_mov_b32_e32 v70, v64
	v_mov_b32_e32 v71, v64
	v_mov_b32_e32 v72, v64
	v_mov_b32_e32 v73, v64
	v_mov_b32_e32 v74, v64
	v_mov_b32_e32 v75, v64
	v_mov_b32_e32 v76, v64
	v_mov_b32_e32 v77, v64
	v_mov_b32_e32 v78, v64
	v_mov_b32_e32 v79, v64
	s_waitcnt lgkmcnt(0)
	v_mfma_f32_32x32x64_f8f6f4 v[112:127], v[96:103], v[176:183], v[64:79]
	v_xad_u32 v132, v132, 16, 0
	v_mfma_f32_32x32x64_f8f6f4 v[112:127], v[104:111], v[184:191], v[112:127]
	v_mfma_f32_32x32x64_f8f6f4 v[96:111], v[158:165], v[176:183], v[64:79]
	v_add_u32_e32 v133, s0, v201
	v_exp_f32_e32 v134, v88
	v_exp_f32_e32 v135, v92
	v_mfma_f32_32x32x64_f8f6f4 v[96:111], v[166:173], v[184:191], v[96:111]
	ds_read_b128 v[162:165], v132
	ds_read_b128 v[158:161], v133 offset:49152
	ds_read_b128 v[166:169], v133 offset:51200
	ds_read_b128 v[170:173], v132 offset:2048
	v_exp_f32_e32 v132, v80
	v_exp_f32_e32 v133, v84
	s_waitcnt lgkmcnt(0)
	v_mfma_f32_32x32x64_f8f6f4 v[112:127], v[158:165], v[192:199], v[112:127]
	v_mfma_f32_32x32x64_f8f6f4 v[96:111], v[166:173], v[192:199], v[96:111]
	v_add_f32_e32 v65, 0, v128
	v_add_f32_e32 v65, v154, v65
	v_add_f32_e32 v65, v136, v65
	v_add_f32_e32 v65, v137, v65
	v_add_f32_e32 v65, v129, v65
	v_add_f32_e32 v65, v155, v65
	v_add_f32_e32 v65, v138, v65
	v_add_f32_e32 v65, v139, v65
	v_add_f32_e32 v65, v130, v65
	v_add_f32_e32 v65, v156, v65
	v_add_f32_e32 v65, v140, v65
	v_add_f32_e32 v65, v141, v65
	v_add_f32_e32 v65, v131, v65
	v_exp_f32_e32 v64, v81
	v_add_f32_e32 v65, v157, v65
	v_exp_f32_e32 v66, v82
	v_add_f32_e32 v65, v142, v65
	v_exp_f32_e32 v67, v83
	v_add_f32_e32 v65, v143, v65
	v_add_f32_e32 v65, v132, v65
	v_exp_f32_e32 v68, v85
	v_add_f32_e32 v65, v64, v65
	v_exp_f32_e32 v69, v86
	v_add_f32_e32 v65, v66, v65
	v_exp_f32_e32 v70, v87
	v_add_f32_e32 v65, v67, v65
	v_add_f32_e32 v65, v133, v65
	v_exp_f32_e32 v71, v89
	v_add_f32_e32 v65, v68, v65
	v_exp_f32_e32 v72, v90
	v_add_f32_e32 v65, v69, v65
	v_exp_f32_e32 v73, v91
	v_add_f32_e32 v65, v70, v65
	v_add_f32_e32 v65, v134, v65
	v_exp_f32_e32 v74, v93
	v_add_f32_e32 v65, v71, v65
	v_exp_f32_e32 v75, v94
	v_add_f32_e32 v65, v72, v65
	v_exp_f32_e32 v76, v95
	v_add_f32_e32 v65, v73, v65
	v_add_f32_e32 v65, v135, v65
	v_add_f32_e32 v65, v74, v65
	v_add_f32_e32 v65, v75, v65
	v_cvt_pk_fp8_f32 v128, v128, v154
	v_cvt_pk_fp8_f32 v129, v129, v155
	v_cvt_pk_fp8_f32 v130, v130, v156
	v_cvt_pk_fp8_f32 v131, v131, v157
	v_cvt_pk_fp8_f32 v132, v132, v64
	v_cvt_pk_fp8_f32 v133, v133, v68
	v_cvt_pk_fp8_f32 v134, v134, v71
	v_cvt_pk_fp8_f32 v135, v135, v74
	v_add_f32_e32 v65, v76, v65
	v_mov_b32_e32 v74, v65
	s_nop 1
	v_permlane32_swap_b32_e32 v65, v74
	v_cvt_pk_fp8_f32 v128, v136, v137 op_sel:[0,0,1]
	v_cvt_pk_fp8_f32 v129, v138, v139 op_sel:[0,0,1]
	v_cvt_pk_fp8_f32 v130, v140, v141 op_sel:[0,0,1]
	v_cvt_pk_fp8_f32 v131, v142, v143 op_sel:[0,0,1]
	v_cvt_pk_fp8_f32 v132, v66, v67 op_sel:[0,0,1]
	v_cvt_pk_fp8_f32 v133, v69, v70 op_sel:[0,0,1]
	v_cvt_pk_fp8_f32 v134, v72, v73 op_sel:[0,0,1]
	v_cvt_pk_fp8_f32 v135, v75, v76 op_sel:[0,0,1]
	v_lshl_add_u32 v64, s3, 14, v152
	v_add_u32_e32 v75, 0, v64
	v_xad_u32 v64, v64, 16, 0
	ds_read_b128 v[66:69], v75
	ds_read_b128 v[76:79], v75 offset:2048
	ds_read_b128 v[70:73], v64
	ds_read_b128 v[80:83], v64 offset:2048
	ds_read_b128 v[84:87], v75 offset:4096
	ds_read_b128 v[136:139], v75 offset:6144
	ds_read_b128 v[88:91], v64 offset:4096
	ds_read_b128 v[140:143], v64 offset:6144
	s_waitcnt lgkmcnt(0)
	s_waitcnt lgkmcnt(0)
	v_mfma_f32_32x32x64_f8f6f4 v[0:15], v[128:135], v[66:73], v[0:15]
	v_max_f32_e32 v64, v113, v113
	v_max_f32_e32 v66, v112, v112
	v_max_f32_e32 v64, v66, v64
	v_max3_f32 v64, v64, v114, v115
	v_max3_f32 v64, v64, v116, v117
	v_max3_f32 v64, v64, v118, v119
	v_max3_f32 v64, v64, v120, v121
	v_max3_f32 v64, v64, v122, v123
	v_max3_f32 v64, v64, v124, v125
	v_max3_f32 v64, v64, v126, v127
	v_max3_f32 v64, v64, v96, v97
	v_max3_f32 v64, v64, v98, v99
	v_max3_f32 v64, v64, v100, v101
	v_max3_f32 v64, v64, v102, v103
	v_max3_f32 v64, v64, v104, v105
	v_mfma_f32_32x32x64_f8f6f4 v[16:31], v[128:135], v[76:83], v[16:31]
	v_max3_f32 v64, v64, v106, v107
	v_max3_f32 v64, v64, v108, v109
	v_max3_f32 v64, v64, v110, v111
	v_mov_b32_e32 v66, v64
	s_nop 1
	v_permlane32_swap_b32_e32 v64, v66
	v_max_f32_e32 v66, v66, v66
	v_max_f32_e32 v64, v64, v64
	v_max_f32_e32 v64, v64, v66
	v_cmp_ge_f32_e32 vcc, s10, v64
	s_cmp_eq_u64 vcc, exec
	v_mov_b32_e32 v75, 1.0
	v_mfma_f32_32x32x64_f8f6f4 v[32:47], v[128:135], v[84:91], v[32:47]
	v_mfma_f32_32x32x64_f8f6f4 v[48:63], v[128:135], v[136:143], v[48:63]
	s_cbranch_scc0 .LBB0_477

; template <int NKS, bool MACC>
; __device__ __forceinline__ void qkt8d(f32x16& p0, f32x16& p1, const f32x16& mneg, LAS unsigned char* ldsl, int kb, int rb, const i32x8* qf) {
;     i32x8 a0[2], a1[2];
; #pragma unroll
;     for (int sK = 0; sK < 2; ++sK) {
;         { const i32x4 lo = LDS16(kb ^ (64 * sK)), hh = LDS16(kb ^ (64 * sK + 16)); a0[sK] = __builtin_shufflevector(lo, hh, 0, 1, 2, 3, 4, 5, 6, 7); }
;         { const i32x4 lo = LDS16((kb ^ (64 * sK)) + 4096), hh = LDS16((kb ^ (64 * sK + 16)) + 4096); a1[sK] = __builtin_shufflevector(lo, hh, 0, 1, 2, 3, 4, 5, 6, 7); } }
;     asm volatile("s_waitcnt lgkmcnt(0)" ::: "memory"); SBAR();
;     if constexpr (MACC) {
;         asm volatile("v_mfma_f32_32x32x64_f8f6f4 %0, %1, %2, %3" : "=&v"(p0) : "v"(a0[0]), "v"(qf[0]), "v"(mneg));
;         asm volatile("v_mfma_f32_32x32x64_f8f6f4 %0, %1, %2, %3" : "=&v"(p1) : "v"(a1[0]), "v"(qf[0]), "v"(mneg)); }
;     else { p0 = f32x16{}; p1 = f32x16{}; p0 = D8_MX(a0[0], qf[0], p0); p1 = D8_MX(a1[0], qf[0], p1); }
;     if constexpr (NKS == 3) { i32x8 r0, r1;
;         { const i32x4 lo = LDS16(rb), hh = LDS16(rb ^ 16); r0 = __builtin_shufflevector(lo, hh, 0, 1, 2, 3, 4, 5, 6, 7); }
;         { const i32x4 lo = LDS16(rb + 2048), hh = LDS16((rb ^ 16) + 2048); r1 = __builtin_shufflevector(lo, hh, 0, 1, 2, 3, 4, 5, 6, 7); }
;         p0 = D8_MX(a0[1], qf[1], p0); p1 = D8_MX(a1[1], qf[1], p1);
;         p0 = D8_MX(r0, qf[2], p0); p1 = D8_MX(r1, qf[2], p1); }
;     else { p0 = D8_MX(a0[1], qf[1], p0); p1 = D8_MX(a1[1], qf[1], p1); }
;     if constexpr (MACC) asm volatile("" : "+v"(p1), "+v"(p0) : "v"(mneg));
; }
; __device__ __forceinline__ void pv8d(f32x16* o, LAS unsigned char* ldsl, int vb, const i32x8 pa) {
;     i32x8 bfr[4];
; #pragma unroll
;     for (int d0 = 0; d0 < 4; ++d0) { const i32x4 lo = LDS16(vb + d0 * 2048), hh = LDS16((vb ^ 16) + d0 * 2048); bfr[d0] = __builtin_shufflevector(lo, hh, 0, 1, 2, 3, 4, 5, 6, 7); }
;     asm volatile("s_waitcnt lgkmcnt(0)" ::: "memory"); SBAR();
; #pragma unroll
;     for (int d0 = 0; d0 < 4; ++d0) o[d0] = D8_MX(pa, bfr[d0], o[d0]);
; }
; template <int NKS, bool MACC>
; __device__ __forceinline__ void attn_dense8_dma(int wv, const D8Args a, LAS unsigned char* ldsl) {
;     ...
;         RESC8(alA);
;         SBAR(); D8Qm(pB0, pB1, 2 * sb + 1);
;         D8Fm(pA0, pA1, alA); SBAR();
;         D8Vm(2 * sb); D8Pm(false, pB0, pB1, alB);
.LBB0_470:
	v_exp_f32_e32 v66, v112
	v_exp_f32_e32 v170, v113
	v_exp_f32_e32 v171, v114
	v_exp_f32_e32 v172, v115
	v_exp_f32_e32 v67, v116
	v_exp_f32_e32 v173, v117
	v_exp_f32_e32 v174, v118
	v_exp_f32_e32 v175, v119
	v_exp_f32_e32 v68, v120
	v_exp_f32_e32 v209, v121
	v_exp_f32_e32 v210, v122
	v_exp_f32_e32 v211, v123
	v_exp_f32_e32 v69, v124
	v_exp_f32_e32 v212, v125
	v_exp_f32_e32 v213, v126
	v_exp_f32_e32 v214, v127
	s_lshl_b32 s0, s15, 1
	s_or_b32 s0, s0, 1
	s_lshl_b32 s1, s0, 13
	v_or_b32_e32 v70, s1, v202
	v_add_u32_e32 v72, 0, v70
	v_xad_u32 v73, v70, 16, 0
	ds_read_b128 v[76:79], v72
	ds_read_b128 v[154:157], v72 offset:4096
	ds_read_b128 v[80:83], v73
	ds_read_b128 v[158:161], v73 offset:4096
	v_xad_u32 v70, v70, 64, 0
	v_bitop3_b32 v72, s1, v242, v202 bitop3:0x36
	v_add_u32_e32 v72, 0, v72
	ds_read_b128 v[84:87], v70
	ds_read_b128 v[162:165], v70 offset:4096
	ds_read_b128 v[88:91], v72
	ds_read_b128 v[166:169], v72 offset:4096
	s_lshl_b32 s0, s0, 12
	v_add_u32_e32 v71, s0, v151
	v_mov_b32_e32 v129, v128
	v_mov_b32_e32 v130, v128
	v_mov_b32_e32 v131, v128
	v_mov_b32_e32 v132, v128
	v_mov_b32_e32 v133, v128
	v_mov_b32_e32 v134, v128
	v_mov_b32_e32 v135, v128
	v_mov_b32_e32 v136, v128
	v_mov_b32_e32 v137, v128
	v_mov_b32_e32 v138, v128
	v_mov_b32_e32 v139, v128
	v_mov_b32_e32 v140, v128
	v_mov_b32_e32 v141, v128
	v_mov_b32_e32 v142, v128
	v_mov_b32_e32 v143, v128
	s_waitcnt lgkmcnt(0)
	v_mfma_f32_32x32x64_f8f6f4 v[112:127], v[76:83], v[176:183], v[128:143]
	v_add_f32_e32 v77, 0, v66
	v_add_f32_e32 v77, v170, v77
	v_add_f32_e32 v77, v171, v77
	v_add_f32_e32 v77, v172, v77
	v_add_f32_e32 v77, v67, v77
	v_add_f32_e32 v77, v173, v77
	v_add_f32_e32 v77, v174, v77
	v_add_f32_e32 v77, v175, v77
	v_add_f32_e32 v77, v68, v77
	v_add_f32_e32 v77, v209, v77
	v_add_f32_e32 v77, v210, v77
	v_mfma_f32_32x32x64_f8f6f4 v[112:127], v[84:91], v[184:191], v[112:127]
	v_mfma_f32_32x32x64_f8f6f4 v[80:95], v[154:161], v[176:183], v[128:143]
	v_add_u32_e32 v70, s0, v201
	v_xad_u32 v71, v71, 16, 0
	v_add_f32_e32 v77, v211, v77
	v_add_f32_e32 v77, v69, v77
	v_exp_f32_e32 v76, v97
	v_add_f32_e32 v77, v212, v77
	v_exp_f32_e32 v78, v98
	v_add_f32_e32 v77, v213, v77
	v_exp_f32_e32 v79, v99
	v_add_f32_e32 v77, v214, v77
	v_exp_f32_e32 v97, v102
	v_exp_f32_e32 v98, v103
	v_exp_f32_e32 v72, v104
	v_exp_f32_e32 v99, v105
	v_mfma_f32_32x32x64_f8f6f4 v[80:95], v[162:169], v[184:191], v[80:95]
	ds_read_b128 v[158:161], v71
	ds_read_b128 v[154:157], v70 offset:49152
	ds_read_b128 v[162:165], v70 offset:51200
	ds_read_b128 v[166:169], v71 offset:2048
	v_exp_f32_e32 v70, v96
	v_exp_f32_e32 v71, v100
	v_exp_f32_e32 v96, v101
	v_exp_f32_e32 v100, v106
	v_add_f32_e32 v77, v70, v77
	v_add_f32_e32 v77, v76, v77
	v_add_f32_e32 v77, v78, v77
	v_add_f32_e32 v77, v79, v77
	v_add_f32_e32 v77, v71, v77
	v_add_f32_e32 v77, v96, v77
	v_add_f32_e32 v77, v97, v77
	v_exp_f32_e32 v101, v107
	v_add_f32_e32 v77, v98, v77
	v_exp_f32_e32 v73, v108
	v_add_f32_e32 v77, v72, v77
	v_exp_f32_e32 v102, v109
	v_add_f32_e32 v77, v99, v77
	v_exp_f32_e32 v103, v110
	v_add_f32_e32 v77, v100, v77
	v_exp_f32_e32 v104, v111
	v_add_f32_e32 v77, v101, v77
	v_add_f32_e32 v77, v73, v77
	v_cvt_pk_fp8_f32 v70, v70, v76
	v_add_f32_e32 v77, v102, v77
	v_add_f32_e32 v77, v103, v77
	v_cvt_pk_fp8_f32 v66, v66, v170
	v_cvt_pk_fp8_f32 v67, v67, v173
	v_cvt_pk_fp8_f32 v68, v68, v209
	v_cvt_pk_fp8_f32 v69, v69, v212
	v_cvt_pk_fp8_f32 v71, v71, v96
	v_cvt_pk_fp8_f32 v72, v72, v99
	v_cvt_pk_fp8_f32 v73, v73, v102
	v_add_f32_e32 v77, v104, v77
	v_cvt_pk_fp8_f32 v70, v78, v79 op_sel:[0,0,1]
	v_mov_b32_e32 v78, v77
	s_waitcnt lgkmcnt(0)
	v_mfma_f32_32x32x64_f8f6f4 v[112:127], v[154:161], v[192:199], v[112:127]
	v_permlane32_swap_b32_e32 v77, v78
	v_cvt_pk_fp8_f32 v66, v171, v172 op_sel:[0,0,1]
	v_cvt_pk_fp8_f32 v67, v174, v175 op_sel:[0,0,1]
	v_cvt_pk_fp8_f32 v68, v210, v211 op_sel:[0,0,1]
	v_cvt_pk_fp8_f32 v69, v213, v214 op_sel:[0,0,1]
	v_cvt_pk_fp8_f32 v71, v97, v98 op_sel:[0,0,1]
	v_cvt_pk_fp8_f32 v72, v100, v101 op_sel:[0,0,1]
	v_cvt_pk_fp8_f32 v73, v103, v104 op_sel:[0,0,1]
	v_mfma_f32_32x32x64_f8f6f4 v[80:95], v[162:169], v[192:199], v[80:95]
	v_add_u32_e32 v76, s23, v203
	v_add_u32_e32 v79, s23, v205
	v_xad_u32 v76, v76, 16, 0
	ds_read_b128 v[96:99], v79
	ds_read_b128 v[104:107], v79 offset:2048
	ds_read_b128 v[100:103], v76
	ds_read_b128 v[108:111], v76 offset:2048
	ds_read_b128 v[128:131], v79 offset:4096
	ds_read_b128 v[136:139], v79 offset:6144
	ds_read_b128 v[132:135], v76 offset:4096
	ds_read_b128 v[140:143], v76 offset:6144
	s_waitcnt lgkmcnt(0)
	v_max_f32_e32 v76, v113, v113
	v_max_f32_e32 v79, v112, v112
	v_max_f32_e32 v76, v79, v76
	v_max3_f32 v76, v76, v114, v115
	v_max3_f32 v76, v76, v116, v117
	v_max3_f32 v76, v76, v118, v119
	v_max3_f32 v76, v76, v120, v121
	v_max3_f32 v76, v76, v122, v123
	s_waitcnt lgkmcnt(0)
	v_mfma_f32_32x32x64_f8f6f4 v[0:15], v[66:73], v[96:103], v[0:15]
	v_max3_f32 v76, v76, v124, v125
	v_max3_f32 v76, v76, v126, v127
	v_max3_f32 v76, v76, v80, v81
	v_max3_f32 v76, v76, v82, v83
	v_max3_f32 v76, v76, v84, v85
	v_max3_f32 v76, v76, v86, v87
	v_max3_f32 v76, v76, v88, v89
	v_max3_f32 v76, v76, v90, v91
	v_max3_f32 v76, v76, v92, v93
	v_max3_f32 v76, v76, v94, v95
	v_mov_b32_e32 v79, v76
	s_nop 1
	v_permlane32_swap_b32_e32 v76, v79
	v_max_f32_e32 v79, v79, v79
	v_max_f32_e32 v76, v76, v76
	v_mfma_f32_32x32x64_f8f6f4 v[16:31], v[66:73], v[104:111], v[16:31]
	v_max_f32_e32 v79, v76, v79
	v_cmp_ge_f32_e32 vcc, s10, v79
	s_cmp_eq_u64 vcc, exec
	v_mov_b32_e32 v76, 1.0
	v_mfma_f32_32x32x64_f8f6f4 v[32:47], v[66:73], v[128:135], v[32:47]
	v_mfma_f32_32x32x64_f8f6f4 v[48:63], v[66:73], v[136:143], v[48:63]
	s_cbranch_scc0 .LBB0_478

; __device__ __forceinline__ bf16_t f2bf(float f) { return (bf16_t)(cvtpk(f, f) & 0xffffu); }
; __device__ __forceinline__ unsigned char f2fp8(float v) { return (unsigned char)(__builtin_amdgcn_cvt_pk_fp8_f32(v, v, (int)__float_as_uint(v), false) & 0xff); }
; __device__ __forceinline__ int fresh_tid(int wv) { int l; asm volatile("v_mbcnt_lo_u32_b32 %0, -1, 0\n\tv_mbcnt_hi_u32_b32 %0, -1, %0" : "=v"(l)); return wv * 64 + l; }
; #define SBAR() __builtin_amdgcn_sched_barrier(0)
; __device__ __forceinline__ int crow(int r, int hi) { return (r & 3) + 8 * (r >> 2) + 4 * hi; }
; #define SBAR() __builtin_amdgcn_sched_barrier(0)
; #define D8Vm(b) do { pv8d(o, ldsl, vb0 + (b) * K8_BYTES, pa); if constexpr (LSUM) lacc = D8_MX(pa, ones8, lacc); } while (0)
; #define D8Fm(P0, P1, AL) do { if constexpr (LSUM) finishSM8n(P0, P1, pa); else finishSM8(P0, P1, AL, l_reg, pa); } while (0)
; template <int NKS, bool MACC>
; __device__ __forceinline__ void attn_dense8_dma(int wv, const D8Args a, LAS unsigned char* ldsl) {
;     ...
;     D8Fm(pB0, pB1, alB); SBAR();
;     D8Vm(2 * sbp + 1);
;     const int tid_e = fresh_tid(wv), wid_e = tid_e >> 6, r32e = tid_e & 31, hie = (tid_e >> 5) & 1;
;     float* li_e = (float*)(lds + DM_WS) + wid_e * 64;
;     float rli[16];
;     if constexpr (LSUM) {
; #pragma unroll
;         for (int r = 0; r < 16; ++r) rli[r] = __builtin_amdgcn_rcpf(lacc[r]); (void)li_e; }
;     else { if (hie == 0) li_e[r32e] = l_reg; asm volatile("s_waitcnt lgkmcnt(0)" ::: "memory");
; #pragma unroll
;         for (int r = 0; r < 16; ++r) rli[r] = __builtin_amdgcn_rcpf(li_e[da::crow(r, hie)]); }
;     bf16_t* Ow = F8_OUT ? (bf16_t*)((unsigned char*)a.O + (long)(wid_e * 32) * a.ldo) : a.O + (long)(wid_e * 32) * a.ldo;
; #pragma unroll
;     for (int r = 0; r < 16; ++r) { const int orow = da::crow(r, hie);
; #pragma unroll
;         for (int d0 = 0; d0 < 4; ++d0) { if constexpr (F8_OUT) ((unsigned char*)Ow)[(long)orow * a.ldo + d0 * 32 + r32e] = f2fp8(o[d0][r] * rli[r] * O8_SCALE); else Ow[(long)orow * a.ldo + d0 * 32 + r32e] = f2bf(o[d0][r] * rli[r]); } }
.LBB0_515:
	v_exp_f32_e32 v148, v96
	v_exp_f32_e32 v64, v97
	v_exp_f32_e32 v149, v100
	v_exp_f32_e32 v67, v101
	v_exp_f32_e32 v150, v104
	v_exp_f32_e32 v70, v105
	v_exp_f32_e32 v151, v108
	v_exp_f32_e32 v73, v109
	s_lshl_b64 s[0:1], s[2:3], 11
	v_exp_f32_e32 v65, v98
	v_exp_f32_e32 v66, v99
	v_exp_f32_e32 v68, v102
	v_exp_f32_e32 v69, v103
	v_exp_f32_e32 v71, v106
	v_exp_f32_e32 v72, v107
	v_exp_f32_e32 v74, v110
	v_exp_f32_e32 v75, v111
	v_cvt_pk_fp8_f32 v144, v144, v160
	v_cvt_pk_fp8_f32 v145, v145, v161
	v_cvt_pk_fp8_f32 v146, v146, v162
	v_cvt_pk_fp8_f32 v147, v147, v163
	v_cvt_pk_fp8_f32 v148, v148, v64
	v_cvt_pk_fp8_f32 v149, v149, v67
	v_cvt_pk_fp8_f32 v150, v150, v70
	v_cvt_pk_fp8_f32 v151, v151, v73
	s_add_u32 s0, s70, s0
	s_addc_u32 s1, s71, s1
	s_add_u32 s0, s0, s43
	v_cvt_pk_fp8_f32 v144, v152, v153 op_sel:[0,0,1]
	v_cvt_pk_fp8_f32 v145, v154, v155 op_sel:[0,0,1]
	v_cvt_pk_fp8_f32 v146, v156, v157 op_sel:[0,0,1]
	v_cvt_pk_fp8_f32 v147, v158, v159 op_sel:[0,0,1]
	v_cvt_pk_fp8_f32 v148, v65, v66 op_sel:[0,0,1]
	v_cvt_pk_fp8_f32 v149, v68, v69 op_sel:[0,0,1]
	v_cvt_pk_fp8_f32 v150, v71, v72 op_sel:[0,0,1]
	v_cvt_pk_fp8_f32 v151, v74, v75 op_sel:[0,0,1]
	s_addc_u32 s1, s1, 0
	v_add_u32_e32 v72, 0, v235
	v_xor_b32_e32 v65, 0x18010, v235
	v_add_u32_e32 v64, 0x18000, v72
	v_add_u32_e32 v108, 0, v65
	v_add_u32_e32 v73, 0x18800, v72
	v_add_u32_e32 v74, 0x19000, v72
	v_add_u32_e32 v72, 0x19800, v72
	ds_read_b128 v[64:67], v64
	ds_read_b128 v[68:71], v108
	ds_read_b128 v[76:79], v108 offset:2048
	ds_read_b128 v[100:103], v108 offset:4096
	ds_read_b128 v[96:99], v74
	ds_read_b128 v[104:107], v72
	ds_read_b128 v[72:75], v73
	ds_read_b128 v[108:111], v108 offset:6144
	s_waitcnt lgkmcnt(0)
	v_mov_b32_e32 v209, v208
	v_mov_b32_e32 v210, v208
	v_mov_b32_e32 v211, v208
	v_mov_b32_e32 v212, v208
	v_mov_b32_e32 v213, v208
	v_mov_b32_e32 v214, v208
	v_mov_b32_e32 v215, v208
	s_waitcnt lgkmcnt(0)
	v_mfma_f32_32x32x64_f8f6f4 v[0:15], v[144:151], v[64:71], v[0:15]
	v_mbcnt_lo_u32_b32 v66, -1, 0
	v_mbcnt_hi_u32_b32 v66, -1, v66
	s_add_i32 s42, s42, s50
	v_mfma_f32_32x32x64_f8f6f4 v[80:95], v[144:151], v[208:215], v[80:95]
	v_mfma_f32_32x32x64_f8f6f4 v[16:31], v[144:151], v[72:79], v[16:31]
	v_mfma_f32_32x32x64_f8f6f4 v[32:47], v[144:151], v[96:103], v[32:47]
	v_mfma_f32_32x32x64_f8f6f4 v[48:63], v[144:151], v[104:111], v[48:63]
	v_and_b32_e32 v232, 31, v66
	v_add_u32_e32 v64, s5, v66
	v_lshrrev_b32_e32 v64, 6, v64
	v_lshlrev_b32_e32 v64, 5, v64
	v_bfe_u32 v65, v66, 5, 1
	v_lshl_add_u32 v64, v65, 2, v64
	v_and_b32_e32 v65, 3, v232
	v_add_u32_e32 v64, v64, v65
	v_lshlrev_b32_e32 v64, 11, v64
	v_lshrrev_b32_e32 v65, 2, v232
	v_lshl_add_u32 v64, v65, 2, v64
	v_bfe_i32 v65, v232, 0, 1
	v_and_b32_e32 v65, 0x05050505, v65
	v_xor_b32_e32 v65, 0x06020400, v65
	v_bfe_i32 v66, v232, 1, 1
	v_and_b32_e32 v66, 0x06060606, v66
	v_xor_b32_e32 v66, 0x05040100, v66
	s_nop 7
	v_rcp_f32_e32 v80, v80
	v_rcp_f32_e32 v81, v81
	v_rcp_f32_e32 v82, v82
	v_rcp_f32_e32 v83, v83
	v_rcp_f32_e32 v84, v84
	v_rcp_f32_e32 v85, v85
	v_rcp_f32_e32 v86, v86
	v_rcp_f32_e32 v87, v87
	v_rcp_f32_e32 v88, v88
	v_rcp_f32_e32 v89, v89
	v_rcp_f32_e32 v90, v90
	v_rcp_f32_e32 v91, v91
	v_rcp_f32_e32 v92, v92
	v_rcp_f32_e32 v93, v93
	v_rcp_f32_e32 v94, v94
	v_rcp_f32_e32 v95, v95
	v_mul_f32_e32 v80, 0x41800000, v80
	v_mul_f32_e32 v81, 0x41800000, v81
	v_mul_f32_e32 v82, 0x41800000, v82
	v_mul_f32_e32 v83, 0x41800000, v83
	v_mul_f32_e32 v84, 0x41800000, v84
	v_mul_f32_e32 v85, 0x41800000, v85
	v_mul_f32_e32 v86, 0x41800000, v86
	v_mul_f32_e32 v87, 0x41800000, v87
	v_mul_f32_e32 v88, 0x41800000, v88
	v_mul_f32_e32 v89, 0x41800000, v89
	v_mul_f32_e32 v90, 0x41800000, v90
	v_mul_f32_e32 v91, 0x41800000, v91
	v_mul_f32_e32 v92, 0x41800000, v92
	v_mul_f32_e32 v93, 0x41800000, v93
	v_mul_f32_e32 v94, 0x41800000, v94
	v_mul_f32_e32 v95, 0x41800000, v95
	v_mul_f32_e32 v0, v0, v80
	v_mul_f32_e32 v16, v16, v80
	v_mul_f32_e32 v32, v32, v80
	v_mul_f32_e32 v48, v48, v80
	v_mul_f32_e32 v1, v1, v81
	v_mul_f32_e32 v17, v17, v81
	v_mul_f32_e32 v33, v33, v81
	v_mul_f32_e32 v49, v49, v81
	v_mul_f32_e32 v2, v2, v82
	v_mul_f32_e32 v18, v18, v82
	v_mul_f32_e32 v34, v34, v82
	v_mul_f32_e32 v50, v50, v82
	v_mul_f32_e32 v3, v3, v83
	v_mul_f32_e32 v19, v19, v83
	v_mul_f32_e32 v35, v35, v83
	v_mul_f32_e32 v51, v51, v83
	v_cvt_pk_fp8_f32 v0, v0, v1
	v_cvt_pk_fp8_f32 v16, v16, v17
	v_cvt_pk_fp8_f32 v32, v32, v33
	v_cvt_pk_fp8_f32 v48, v48, v49
	v_cvt_pk_fp8_f32 v0, v2, v3 op_sel:[0,0,1]
	v_cvt_pk_fp8_f32 v16, v18, v19 op_sel:[0,0,1]
	v_cvt_pk_fp8_f32 v32, v34, v35 op_sel:[0,0,1]
	v_cvt_pk_fp8_f32 v48, v50, v51 op_sel:[0,0,1]
	v_mov_b32_dpp v1, v0 quad_perm:[1,0,3,2] row_mask:0xf bank_mask:0xf
	v_mov_b32_dpp v17, v16 quad_perm:[1,0,3,2] row_mask:0xf bank_mask:0xf
	v_mov_b32_dpp v33, v32 quad_perm:[1,0,3,2] row_mask:0xf bank_mask:0xf
	v_mov_b32_dpp v49, v48 quad_perm:[1,0,3,2] row_mask:0xf bank_mask:0xf
	v_perm_b32 v2, v1, v0, v65
	v_perm_b32 v18, v17, v16, v65
	v_perm_b32 v34, v33, v32, v65
	v_perm_b32 v50, v49, v48, v65
	v_mov_b32_dpp v3, v2 quad_perm:[2,3,0,1] row_mask:0xf bank_mask:0xf
	v_mov_b32_dpp v19, v18 quad_perm:[2,3,0,1] row_mask:0xf bank_mask:0xf
	v_mov_b32_dpp v35, v34 quad_perm:[2,3,0,1] row_mask:0xf bank_mask:0xf
	v_mov_b32_dpp v51, v50 quad_perm:[2,3,0,1] row_mask:0xf bank_mask:0xf
	v_perm_b32 v0, v3, v2, v66
	v_perm_b32 v16, v19, v18, v66
	v_perm_b32 v32, v35, v34, v66
	v_perm_b32 v48, v51, v50, v66
	global_store_dword v64, v0, s[0:1] offset:0
	global_store_dword v64, v16, s[0:1] offset:32
	global_store_dword v64, v32, s[0:1] offset:64
; __device__ __forceinline__ bf16_t f2bf(float f) { return (bf16_t)(cvtpk(f, f) & 0xffffu); }
; __device__ __forceinline__ unsigned char f2fp8(float v) { return (unsigned char)(__builtin_amdgcn_cvt_pk_fp8_f32(v, v, (int)__float_as_uint(v), false) & 0xff); }
; __device__ __forceinline__ int crow(int r, int hi) { return (r & 3) + 8 * (r >> 2) + 4 * hi; }
; template <int NKS, bool MACC>
; __device__ __forceinline__ void attn_dense8_dma(int wv, const D8Args a, LAS unsigned char* ldsl) {
;     ...
;     for (int r = 0; r < 16; ++r) { const int orow = da::crow(r, hie);
; #pragma unroll
;         for (int d0 = 0; d0 < 4; ++d0) { if constexpr (F8_OUT) ((unsigned char*)Ow)[(long)orow * a.ldo + d0 * 32 + r32e] = f2fp8(o[d0][r] * rli[r] * O8_SCALE); else Ow[(long)orow * a.ldo + d0 * 32 + r32e] = f2bf(o[d0][r] * rli[r]); } }
; __global__ void __launch_bounds__(NTHR, 2) fwd(Params p) {
;     ...
;                 for (int u = vcu; u < 1024; u += G) {
	global_store_dword v64, v48, s[0:1] offset:96
	s_add_u32 s0, s0, 0x4000
	s_addc_u32 s1, s1, 0
	v_mul_f32_e32 v4, v4, v84
	v_mul_f32_e32 v20, v20, v84
	v_mul_f32_e32 v36, v36, v84
	v_mul_f32_e32 v52, v52, v84
	v_mul_f32_e32 v5, v5, v85
	v_mul_f32_e32 v21, v21, v85
	v_mul_f32_e32 v37, v37, v85
	v_mul_f32_e32 v53, v53, v85
	v_mul_f32_e32 v6, v6, v86
	v_mul_f32_e32 v22, v22, v86
	v_mul_f32_e32 v38, v38, v86
	v_mul_f32_e32 v54, v54, v86
	v_mul_f32_e32 v7, v7, v87
	v_mul_f32_e32 v23, v23, v87
	v_mul_f32_e32 v39, v39, v87
	v_mul_f32_e32 v55, v55, v87
	v_cvt_pk_fp8_f32 v4, v4, v5
	v_cvt_pk_fp8_f32 v20, v20, v21
	v_cvt_pk_fp8_f32 v36, v36, v37
	v_cvt_pk_fp8_f32 v52, v52, v53
	v_cvt_pk_fp8_f32 v4, v6, v7 op_sel:[0,0,1]
	v_cvt_pk_fp8_f32 v20, v22, v23 op_sel:[0,0,1]
	v_cvt_pk_fp8_f32 v36, v38, v39 op_sel:[0,0,1]
	v_cvt_pk_fp8_f32 v52, v54, v55 op_sel:[0,0,1]
	v_mov_b32_dpp v5, v4 quad_perm:[1,0,3,2] row_mask:0xf bank_mask:0xf
	v_mov_b32_dpp v21, v20 quad_perm:[1,0,3,2] row_mask:0xf bank_mask:0xf
	v_mov_b32_dpp v37, v36 quad_perm:[1,0,3,2] row_mask:0xf bank_mask:0xf
	v_mov_b32_dpp v53, v52 quad_perm:[1,0,3,2] row_mask:0xf bank_mask:0xf
	v_perm_b32 v6, v5, v4, v65
	v_perm_b32 v22, v21, v20, v65
	v_perm_b32 v38, v37, v36, v65
	v_perm_b32 v54, v53, v52, v65
	v_mov_b32_dpp v7, v6 quad_perm:[2,3,0,1] row_mask:0xf bank_mask:0xf
	v_mov_b32_dpp v23, v22 quad_perm:[2,3,0,1] row_mask:0xf bank_mask:0xf
	v_mov_b32_dpp v39, v38 quad_perm:[2,3,0,1] row_mask:0xf bank_mask:0xf
	v_mov_b32_dpp v55, v54 quad_perm:[2,3,0,1] row_mask:0xf bank_mask:0xf
	v_perm_b32 v4, v7, v6, v66
	v_perm_b32 v20, v23, v22, v66
	v_perm_b32 v36, v39, v38, v66
	v_perm_b32 v52, v55, v54, v66
	global_store_dword v64, v4, s[0:1] offset:0
	global_store_dword v64, v20, s[0:1] offset:32
	global_store_dword v64, v36, s[0:1] offset:64
	global_store_dword v64, v52, s[0:1] offset:96
	s_add_u32 s0, s0, 0x4000
	s_addc_u32 s1, s1, 0
	v_mul_f32_e32 v8, v8, v88
	v_mul_f32_e32 v24, v24, v88
	v_mul_f32_e32 v40, v40, v88
	v_mul_f32_e32 v56, v56, v88
	v_mul_f32_e32 v9, v9, v89
	v_mul_f32_e32 v25, v25, v89
	v_mul_f32_e32 v41, v41, v89
	v_mul_f32_e32 v57, v57, v89
	v_mul_f32_e32 v10, v10, v90
	v_mul_f32_e32 v26, v26, v90
	v_mul_f32_e32 v42, v42, v90
	v_mul_f32_e32 v58, v58, v90
	v_mul_f32_e32 v11, v11, v91
	v_mul_f32_e32 v27, v27, v91
	v_mul_f32_e32 v43, v43, v91
	v_mul_f32_e32 v59, v59, v91
	v_cvt_pk_fp8_f32 v8, v8, v9
	v_cvt_pk_fp8_f32 v24, v24, v25
	v_cvt_pk_fp8_f32 v40, v40, v41
	v_cvt_pk_fp8_f32 v56, v56, v57
	v_cvt_pk_fp8_f32 v8, v10, v11 op_sel:[0,0,1]
	v_cvt_pk_fp8_f32 v24, v26, v27 op_sel:[0,0,1]
	v_cvt_pk_fp8_f32 v40, v42, v43 op_sel:[0,0,1]
	v_cvt_pk_fp8_f32 v56, v58, v59 op_sel:[0,0,1]
	v_mov_b32_dpp v9, v8 quad_perm:[1,0,3,2] row_mask:0xf bank_mask:0xf
	v_mov_b32_dpp v25, v24 quad_perm:[1,0,3,2] row_mask:0xf bank_mask:0xf
	v_mov_b32_dpp v41, v40 quad_perm:[1,0,3,2] row_mask:0xf bank_mask:0xf
	v_mov_b32_dpp v57, v56 quad_perm:[1,0,3,2] row_mask:0xf bank_mask:0xf
	v_perm_b32 v10, v9, v8, v65
	v_perm_b32 v26, v25, v24, v65
	v_perm_b32 v42, v41, v40, v65
	v_perm_b32 v58, v57, v56, v65
	v_mov_b32_dpp v11, v10 quad_perm:[2,3,0,1] row_mask:0xf bank_mask:0xf
	v_mov_b32_dpp v27, v26 quad_perm:[2,3,0,1] row_mask:0xf bank_mask:0xf
	v_mov_b32_dpp v43, v42 quad_perm:[2,3,0,1] row_mask:0xf bank_mask:0xf
	v_mov_b32_dpp v59, v58 quad_perm:[2,3,0,1] row_mask:0xf bank_mask:0xf
	v_perm_b32 v8, v11, v10, v66
	v_perm_b32 v24, v27, v26, v66
	v_perm_b32 v40, v43, v42, v66
	v_perm_b32 v56, v59, v58, v66
	global_store_dword v64, v8, s[0:1] offset:0
	global_store_dword v64, v24, s[0:1] offset:32
	global_store_dword v64, v40, s[0:1] offset:64
	global_store_dword v64, v56, s[0:1] offset:96
	s_add_u32 s0, s0, 0x4000
	s_addc_u32 s1, s1, 0
	v_mul_f32_e32 v12, v12, v92
	v_mul_f32_e32 v28, v28, v92
	v_mul_f32_e32 v44, v44, v92
	v_mul_f32_e32 v60, v60, v92
	v_mul_f32_e32 v13, v13, v93
	v_mul_f32_e32 v29, v29, v93
	v_mul_f32_e32 v45, v45, v93
	v_mul_f32_e32 v61, v61, v93
	v_mul_f32_e32 v14, v14, v94
	v_mul_f32_e32 v30, v30, v94
	v_mul_f32_e32 v46, v46, v94
	v_mul_f32_e32 v62, v62, v94
	v_mul_f32_e32 v15, v15, v95
	v_mul_f32_e32 v31, v31, v95
	v_mul_f32_e32 v47, v47, v95
	v_mul_f32_e32 v63, v63, v95
	v_cvt_pk_fp8_f32 v12, v12, v13
	v_cvt_pk_fp8_f32 v28, v28, v29
	v_cvt_pk_fp8_f32 v44, v44, v45
	v_cvt_pk_fp8_f32 v60, v60, v61
	v_cvt_pk_fp8_f32 v12, v14, v15 op_sel:[0,0,1]
	v_cvt_pk_fp8_f32 v28, v30, v31 op_sel:[0,0,1]
	v_cvt_pk_fp8_f32 v44, v46, v47 op_sel:[0,0,1]
	v_cvt_pk_fp8_f32 v60, v62, v63 op_sel:[0,0,1]
	v_mov_b32_dpp v13, v12 quad_perm:[1,0,3,2] row_mask:0xf bank_mask:0xf
	v_mov_b32_dpp v29, v28 quad_perm:[1,0,3,2] row_mask:0xf bank_mask:0xf
	v_mov_b32_dpp v45, v44 quad_perm:[1,0,3,2] row_mask:0xf bank_mask:0xf
	v_mov_b32_dpp v61, v60 quad_perm:[1,0,3,2] row_mask:0xf bank_mask:0xf
	v_perm_b32 v14, v13, v12, v65
	v_perm_b32 v30, v29, v28, v65
	v_perm_b32 v46, v45, v44, v65
	v_perm_b32 v62, v61, v60, v65
	v_mov_b32_dpp v15, v14 quad_perm:[2,3,0,1] row_mask:0xf bank_mask:0xf
	v_mov_b32_dpp v31, v30 quad_perm:[2,3,0,1] row_mask:0xf bank_mask:0xf
	v_mov_b32_dpp v47, v46 quad_perm:[2,3,0,1] row_mask:0xf bank_mask:0xf
	v_mov_b32_dpp v63, v62 quad_perm:[2,3,0,1] row_mask:0xf bank_mask:0xf
	v_perm_b32 v12, v15, v14, v66
	v_perm_b32 v28, v31, v30, v66
	v_perm_b32 v44, v47, v46, v66
	v_perm_b32 v60, v63, v62, v66
	global_store_dword v64, v12, s[0:1] offset:0
	global_store_dword v64, v28, s[0:1] offset:32
	global_store_dword v64, v44, s[0:1] offset:64
	global_store_dword v64, v60, s[0:1] offset:96
	s_cmpk_gt_i32 s42, 0x3ff
	s_cbranch_scc1 .LBB0_541

; template <int NKS, bool MACC>
; __device__ __forceinline__ void qkt8d(f32x16& p0, f32x16& p1, const f32x16& mneg, LAS unsigned char* ldsl, int kb, int rb, const i32x8* qf) {
;     i32x8 a0[2], a1[2];
; #pragma unroll
;     for (int sK = 0; sK < 2; ++sK) {
;         { const i32x4 lo = LDS16(kb ^ (64 * sK)), hh = LDS16(kb ^ (64 * sK + 16)); a0[sK] = __builtin_shufflevector(lo, hh, 0, 1, 2, 3, 4, 5, 6, 7); }
;         { const i32x4 lo = LDS16((kb ^ (64 * sK)) + 4096), hh = LDS16((kb ^ (64 * sK + 16)) + 4096); a1[sK] = __builtin_shufflevector(lo, hh, 0, 1, 2, 3, 4, 5, 6, 7); } }
;     asm volatile("s_waitcnt lgkmcnt(0)" ::: "memory"); SBAR();
;     if constexpr (MACC) {
;         asm volatile("v_mfma_f32_32x32x64_f8f6f4 %0, %1, %2, %3" : "=&v"(p0) : "v"(a0[0]), "v"(qf[0]), "v"(mneg));
;         asm volatile("v_mfma_f32_32x32x64_f8f6f4 %0, %1, %2, %3" : "=&v"(p1) : "v"(a1[0]), "v"(qf[0]), "v"(mneg)); }
;     else { p0 = f32x16{}; p1 = f32x16{}; p0 = D8_MX(a0[0], qf[0], p0); p1 = D8_MX(a1[0], qf[0], p1); }
;     if constexpr (NKS == 3) { i32x8 r0, r1;
;         { const i32x4 lo = LDS16(rb), hh = LDS16(rb ^ 16); r0 = __builtin_shufflevector(lo, hh, 0, 1, 2, 3, 4, 5, 6, 7); }
;         { const i32x4 lo = LDS16(rb + 2048), hh = LDS16((rb ^ 16) + 2048); r1 = __builtin_shufflevector(lo, hh, 0, 1, 2, 3, 4, 5, 6, 7); }
;         p0 = D8_MX(a0[1], qf[1], p0); p1 = D8_MX(a1[1], qf[1], p1);
;         p0 = D8_MX(r0, qf[2], p0); p1 = D8_MX(r1, qf[2], p1); }
;     else { p0 = D8_MX(a0[1], qf[1], p0); p1 = D8_MX(a1[1], qf[1], p1); }
;     if constexpr (MACC) asm volatile("" : "+v"(p1), "+v"(p0) : "v"(mneg));
; }
; __device__ __forceinline__ void pv8d(f32x16* o, LAS unsigned char* ldsl, int vb, const i32x8 pa) {
;     i32x8 bfr[4];
; #pragma unroll
;     for (int d0 = 0; d0 < 4; ++d0) { const i32x4 lo = LDS16(vb + d0 * 2048), hh = LDS16((vb ^ 16) + d0 * 2048); bfr[d0] = __builtin_shufflevector(lo, hh, 0, 1, 2, 3, 4, 5, 6, 7); }
;     asm volatile("s_waitcnt lgkmcnt(0)" ::: "memory"); SBAR();
; #pragma unroll
;     for (int d0 = 0; d0 < 4; ++d0) o[d0] = D8_MX(pa, bfr[d0], o[d0]);
; }
; template <int NKS, bool MACC>
; __device__ __forceinline__ void attn_dense8_dma(int wv, const D8Args a, LAS unsigned char* ldsl) {
;     ...
;         SBAR(); D8Qm(pA0, pA1, 2 * sb);
;         D8Fm(pB0, pB1, alB); SBAR();
;         D8Vm(2 * sbp + 1); D8Pm(false, pA0, pA1, alA);
;         RESC8(alA);
.LBB0_525:
	s_lshl_b32 s23, s34, 14
	v_or_b32_e32 v112, s23, v248
	v_bitop3_b32 v120, s23, 64, v248 bitop3:0x36
	v_add_u32_e32 v164, 0, v112
	v_bitop3_b32 v112, s23, 16, v248 bitop3:0x36
	v_add_u32_e32 v166, 0, v120
	v_bitop3_b32 v120, s23, v242, v248 bitop3:0x36
	v_add_u32_e32 v165, 0, v112
	ds_read_b128 v[112:115], v164
	ds_read_b128 v[174:177], v164 offset:4096
	ds_read_b128 v[116:119], v165
	ds_read_b128 v[178:181], v165 offset:4096
	v_add_u32_e32 v167, 0, v120
	ds_read_b128 v[182:185], v166
	ds_read_b128 v[190:193], v166 offset:4096
	ds_read_b128 v[186:189], v167
	ds_read_b128 v[194:197], v167 offset:4096
	v_exp_f32_e32 v148, v96
	v_exp_f32_e32 v96, v97
	v_exp_f32_e32 v97, v98
	v_exp_f32_e32 v98, v99
	v_exp_f32_e32 v149, v100
	v_exp_f32_e32 v99, v101
	v_exp_f32_e32 v100, v102
	v_exp_f32_e32 v150, v104
	v_exp_f32_e32 v102, v105
	v_exp_f32_e32 v151, v108
	v_exp_f32_e32 v105, v109
	v_exp_f32_e32 v101, v103
	v_exp_f32_e32 v103, v106
	v_exp_f32_e32 v104, v107
	v_exp_f32_e32 v106, v110
	v_exp_f32_e32 v107, v111
	v_cvt_pk_fp8_f32 v144, v144, v160
	v_cvt_pk_fp8_f32 v145, v145, v161
	v_cvt_pk_fp8_f32 v146, v146, v162
	v_cvt_pk_fp8_f32 v147, v147, v163
	v_cvt_pk_fp8_f32 v148, v148, v96
	v_cvt_pk_fp8_f32 v149, v149, v99
	v_cvt_pk_fp8_f32 v150, v150, v102
	v_cvt_pk_fp8_f32 v151, v151, v105
	s_waitcnt lgkmcnt(0)
	v_mfma_f32_32x32x64_f8f6f4 v[128:143], v[112:119], v[216:223], v[64:79]
	v_mfma_f32_32x32x64_f8f6f4 v[112:127], v[174:181], v[216:223], v[64:79]
	v_cvt_pk_fp8_f32 v144, v152, v153 op_sel:[0,0,1]
	v_mfma_f32_32x32x64_f8f6f4 v[128:143], v[182:189], v[224:231], v[128:143]
	v_cvt_pk_fp8_f32 v145, v154, v155 op_sel:[0,0,1]
	v_cvt_pk_fp8_f32 v146, v156, v157 op_sel:[0,0,1]
	v_cvt_pk_fp8_f32 v147, v158, v159 op_sel:[0,0,1]
	v_cvt_pk_fp8_f32 v148, v97, v98 op_sel:[0,0,1]
	v_cvt_pk_fp8_f32 v149, v100, v101 op_sel:[0,0,1]
	v_cvt_pk_fp8_f32 v150, v103, v104 op_sel:[0,0,1]
	v_cvt_pk_fp8_f32 v151, v106, v107 op_sel:[0,0,1]
	v_mfma_f32_32x32x64_f8f6f4 v[112:127], v[190:197], v[224:231], v[112:127]
	v_lshl_add_u32 v96, s15, 14, v172
	v_add_u32_e32 v156, 0, v96
	v_xad_u32 v160, v96, 16, 0
	ds_read_b128 v[96:99], v156
	ds_read_b128 v[104:107], v156 offset:2048
	ds_read_b128 v[100:103], v160
	ds_read_b128 v[108:111], v160 offset:2048
	ds_read_b128 v[152:155], v156 offset:4096
	ds_read_b128 v[174:177], v156 offset:6144
	ds_read_b128 v[156:159], v160 offset:4096
	ds_read_b128 v[178:181], v160 offset:6144
	s_waitcnt lgkmcnt(0)
	s_waitcnt lgkmcnt(0)
	v_mfma_f32_32x32x64_f8f6f4 v[0:15], v[144:151], v[96:103], v[0:15]
	v_max_f32_e32 v96, v129, v129
	v_max_f32_e32 v97, v128, v128
	v_max_f32_e32 v96, v97, v96
	v_max3_f32 v96, v96, v130, v131
	v_max3_f32 v96, v96, v132, v133
	v_max3_f32 v96, v96, v134, v135
	v_max3_f32 v96, v96, v136, v137
	v_mov_b32_e32 v209, v208
	v_mov_b32_e32 v210, v208
	v_mov_b32_e32 v211, v208
	v_mov_b32_e32 v212, v208
	v_mov_b32_e32 v213, v208
	v_mov_b32_e32 v214, v208
	v_mov_b32_e32 v215, v208
	v_max3_f32 v96, v96, v138, v139
	v_mfma_f32_32x32x64_f8f6f4 v[16:31], v[144:151], v[104:111], v[16:31]
	v_max3_f32 v96, v96, v140, v141
	v_max3_f32 v96, v96, v142, v143
	v_max3_f32 v96, v96, v112, v113
	v_max3_f32 v96, v96, v114, v115
	v_max3_f32 v96, v96, v116, v117
	v_max3_f32 v96, v96, v118, v119
	v_max3_f32 v96, v96, v120, v121
	v_max3_f32 v96, v96, v122, v123
	v_max3_f32 v96, v96, v124, v125
	v_max3_f32 v96, v96, v126, v127
	v_mov_b32_e32 v97, v96
	s_nop 1
	v_permlane32_swap_b32_e32 v96, v97
	v_max_f32_e32 v97, v97, v97
	v_max_f32_e32 v96, v96, v96
	v_mfma_f32_32x32x64_f8f6f4 v[32:47], v[144:151], v[152:159], v[32:47]
	v_max_f32_e32 v96, v96, v97
	v_cmp_ge_f32_e32 vcc, s10, v96
	s_cmp_eq_u64 vcc, exec
	v_mfma_f32_32x32x64_f8f6f4 v[48:63], v[144:151], v[174:181], v[48:63]
	v_mfma_f32_32x32x64_f8f6f4 v[80:95], v[144:151], v[208:215], v[80:95]
	s_cbranch_scc0 .LBB0_537
	v_mov_b64_e32 v[158:159], v[78:79]
	v_mov_b32_e32 v96, 1.0
	v_mov_b64_e32 v[156:157], v[76:77]
	v_mov_b64_e32 v[154:155], v[74:75]
	v_mov_b64_e32 v[152:153], v[72:73]
	v_mov_b64_e32 v[150:151], v[70:71]
	v_mov_b64_e32 v[148:149], v[68:69]
	v_mov_b64_e32 v[146:147], v[66:67]
	v_mov_b64_e32 v[144:145], v[64:65]
	v_cmp_gt_f32_e32 vcc, 1.0, v96
	s_cbranch_vccz .LBB0_530

; template <int NKS, bool MACC>
; __device__ __forceinline__ void qkt8d(f32x16& p0, f32x16& p1, const f32x16& mneg, LAS unsigned char* ldsl, int kb, int rb, const i32x8* qf) {
;     i32x8 a0[2], a1[2];
; #pragma unroll
;     for (int sK = 0; sK < 2; ++sK) {
;         { const i32x4 lo = LDS16(kb ^ (64 * sK)), hh = LDS16(kb ^ (64 * sK + 16)); a0[sK] = __builtin_shufflevector(lo, hh, 0, 1, 2, 3, 4, 5, 6, 7); }
;         { const i32x4 lo = LDS16((kb ^ (64 * sK)) + 4096), hh = LDS16((kb ^ (64 * sK + 16)) + 4096); a1[sK] = __builtin_shufflevector(lo, hh, 0, 1, 2, 3, 4, 5, 6, 7); } }
;     asm volatile("s_waitcnt lgkmcnt(0)" ::: "memory"); SBAR();
;     if constexpr (MACC) {
;         asm volatile("v_mfma_f32_32x32x64_f8f6f4 %0, %1, %2, %3" : "=&v"(p0) : "v"(a0[0]), "v"(qf[0]), "v"(mneg));
;         asm volatile("v_mfma_f32_32x32x64_f8f6f4 %0, %1, %2, %3" : "=&v"(p1) : "v"(a1[0]), "v"(qf[0]), "v"(mneg)); }
;     else { p0 = f32x16{}; p1 = f32x16{}; p0 = D8_MX(a0[0], qf[0], p0); p1 = D8_MX(a1[0], qf[0], p1); }
;     if constexpr (NKS == 3) { i32x8 r0, r1;
;         { const i32x4 lo = LDS16(rb), hh = LDS16(rb ^ 16); r0 = __builtin_shufflevector(lo, hh, 0, 1, 2, 3, 4, 5, 6, 7); }
;         { const i32x4 lo = LDS16(rb + 2048), hh = LDS16((rb ^ 16) + 2048); r1 = __builtin_shufflevector(lo, hh, 0, 1, 2, 3, 4, 5, 6, 7); }
;         p0 = D8_MX(a0[1], qf[1], p0); p1 = D8_MX(a1[1], qf[1], p1);
;         p0 = D8_MX(r0, qf[2], p0); p1 = D8_MX(r1, qf[2], p1); }
;     else { p0 = D8_MX(a0[1], qf[1], p0); p1 = D8_MX(a1[1], qf[1], p1); }
;     if constexpr (MACC) asm volatile("" : "+v"(p1), "+v"(p0) : "v"(mneg));
; }
; __device__ __forceinline__ void pv8d(f32x16* o, LAS unsigned char* ldsl, int vb, const i32x8 pa) {
;     i32x8 bfr[4];
; #pragma unroll
;     for (int d0 = 0; d0 < 4; ++d0) { const i32x4 lo = LDS16(vb + d0 * 2048), hh = LDS16((vb ^ 16) + d0 * 2048); bfr[d0] = __builtin_shufflevector(lo, hh, 0, 1, 2, 3, 4, 5, 6, 7); }
;     asm volatile("s_waitcnt lgkmcnt(0)" ::: "memory"); SBAR();
; #pragma unroll
;     for (int d0 = 0; d0 < 4; ++d0) o[d0] = D8_MX(pa, bfr[d0], o[d0]);
; }
; template <int NKS, bool MACC>
; __device__ __forceinline__ void attn_dense8_dma(int wv, const D8Args a, LAS unsigned char* ldsl) {
;     ...
;         RESC8(alA);
;         SBAR(); D8Qm(pB0, pB1, 2 * sb + 1);
;         D8Fm(pA0, pA1, alA); SBAR();
;         D8Vm(2 * sb); D8Pm(false, pB0, pB1, alB);
.LBB0_530:
	v_exp_f32_e32 v160, v128
	v_exp_f32_e32 v198, v129
	v_exp_f32_e32 v199, v130
	v_exp_f32_e32 v200, v131
	v_exp_f32_e32 v161, v132
	v_exp_f32_e32 v201, v133
	v_exp_f32_e32 v202, v134
	v_exp_f32_e32 v203, v135
	v_exp_f32_e32 v162, v136
	v_exp_f32_e32 v204, v137
	v_exp_f32_e32 v205, v138
	v_exp_f32_e32 v206, v139
	v_exp_f32_e32 v163, v140
	v_exp_f32_e32 v207, v141
	v_exp_f32_e32 v209, v142
	v_exp_f32_e32 v210, v143
	ds_read_b128 v[96:99], v164 offset:8192
	ds_read_b128 v[174:177], v164 offset:12288
	ds_read_b128 v[100:103], v165 offset:8192
	ds_read_b128 v[178:181], v165 offset:12288
	ds_read_b128 v[182:185], v166 offset:8192
	ds_read_b128 v[190:193], v166 offset:12288
	ds_read_b128 v[186:189], v167 offset:8192
	ds_read_b128 v[194:197], v167 offset:12288
	v_exp_f32_e32 v164, v112
	v_exp_f32_e32 v112, v113
	v_exp_f32_e32 v113, v114
	v_exp_f32_e32 v114, v115
	v_exp_f32_e32 v165, v116
	v_exp_f32_e32 v115, v117
	v_exp_f32_e32 v116, v118
	v_exp_f32_e32 v166, v120
	v_exp_f32_e32 v118, v121
	v_exp_f32_e32 v167, v124
	v_exp_f32_e32 v121, v125
	v_exp_f32_e32 v117, v119
	v_exp_f32_e32 v119, v122
	v_exp_f32_e32 v120, v123
	v_exp_f32_e32 v122, v126
	v_exp_f32_e32 v123, v127
	v_cvt_pk_fp8_f32 v160, v160, v198
	v_cvt_pk_fp8_f32 v161, v161, v201
	v_cvt_pk_fp8_f32 v162, v162, v204
	v_cvt_pk_fp8_f32 v163, v163, v207
	v_cvt_pk_fp8_f32 v164, v164, v112
	v_cvt_pk_fp8_f32 v165, v165, v115
	v_cvt_pk_fp8_f32 v166, v166, v118
	v_cvt_pk_fp8_f32 v167, v167, v121
	s_waitcnt lgkmcnt(0)
	v_mfma_f32_32x32x64_f8f6f4 v[128:143], v[96:103], v[216:223], v[144:159]
	v_mfma_f32_32x32x64_f8f6f4 v[96:111], v[174:181], v[216:223], v[144:159]
	v_cvt_pk_fp8_f32 v160, v199, v200 op_sel:[0,0,1]
	v_mfma_f32_32x32x64_f8f6f4 v[128:143], v[182:189], v[224:231], v[128:143]
	v_cvt_pk_fp8_f32 v161, v202, v203 op_sel:[0,0,1]
	v_cvt_pk_fp8_f32 v162, v205, v206 op_sel:[0,0,1]
	v_cvt_pk_fp8_f32 v163, v209, v210 op_sel:[0,0,1]
	v_cvt_pk_fp8_f32 v164, v113, v114 op_sel:[0,0,1]
	v_cvt_pk_fp8_f32 v165, v116, v117 op_sel:[0,0,1]
	v_cvt_pk_fp8_f32 v166, v119, v120 op_sel:[0,0,1]
	v_cvt_pk_fp8_f32 v167, v122, v123 op_sel:[0,0,1]
	v_mfma_f32_32x32x64_f8f6f4 v[96:111], v[190:197], v[224:231], v[96:111]
	v_add_u32_e32 v112, s23, v249
	v_add_u32_e32 v148, s23, v251
	v_xad_u32 v156, v112, 16, 0
	ds_read_b128 v[112:115], v148
	ds_read_b128 v[120:123], v148 offset:2048
	ds_read_b128 v[116:119], v156
	ds_read_b128 v[124:127], v156 offset:2048
	ds_read_b128 v[144:147], v148 offset:4096
	ds_read_b128 v[152:155], v148 offset:6144
	ds_read_b128 v[148:151], v156 offset:4096
	ds_read_b128 v[156:159], v156 offset:6144
	s_waitcnt lgkmcnt(0)
	s_waitcnt lgkmcnt(0)
	v_mfma_f32_32x32x64_f8f6f4 v[0:15], v[160:167], v[112:119], v[0:15]
	v_max_f32_e32 v112, v129, v129
	v_max_f32_e32 v113, v128, v128
	v_max_f32_e32 v112, v113, v112
	v_max3_f32 v112, v112, v130, v131
	v_max3_f32 v112, v112, v132, v133
	v_max3_f32 v112, v112, v134, v135
	v_max3_f32 v112, v112, v136, v137
	v_mov_b32_e32 v209, v208
	v_mov_b32_e32 v210, v208
	v_mov_b32_e32 v211, v208
	v_mov_b32_e32 v212, v208
	v_mov_b32_e32 v213, v208
	v_mov_b32_e32 v214, v208
	v_mov_b32_e32 v215, v208
	v_max3_f32 v112, v112, v138, v139
	v_mfma_f32_32x32x64_f8f6f4 v[16:31], v[160:167], v[120:127], v[16:31]
	v_max3_f32 v112, v112, v140, v141
	v_max3_f32 v112, v112, v142, v143
	v_max3_f32 v112, v112, v96, v97
	v_max3_f32 v112, v112, v98, v99
	v_max3_f32 v112, v112, v100, v101
	v_max3_f32 v112, v112, v102, v103
	v_max3_f32 v112, v112, v104, v105
	v_max3_f32 v112, v112, v106, v107
	v_max3_f32 v112, v112, v108, v109
	v_max3_f32 v112, v112, v110, v111
	v_mov_b32_e32 v113, v112
	s_nop 1
	v_permlane32_swap_b32_e32 v112, v113
	v_max_f32_e32 v113, v113, v113
	v_max_f32_e32 v112, v112, v112
	v_mfma_f32_32x32x64_f8f6f4 v[32:47], v[160:167], v[144:151], v[32:47]
	v_max_f32_e32 v113, v112, v113
	v_cmp_ge_f32_e32 vcc, s10, v113
	s_cmp_eq_u64 vcc, exec
	v_mov_b32_e32 v112, 1.0
	v_mfma_f32_32x32x64_f8f6f4 v[48:63], v[160:167], v[152:159], v[48:63]
	v_mfma_f32_32x32x64_f8f6f4 v[80:95], v[160:167], v[208:215], v[80:95]
	s_cbranch_scc0 .LBB0_538
	v_cmp_gt_f32_e32 vcc, 1.0, v112
	s_cbranch_vccz .LBB0_535
